# GQA loop unrolled over the LDS ring (immediate ring offsets), tile-load address math as before
# speedup vs baseline: 1.0073x; 1.0073x over previous
; __device__ __forceinline__ unsigned cvt_pk_bf16(float lo, float hi) { unsigned r; asm volatile("v_cvt_pk_bf16_f32 %0, %1, %2" : "=v"(r) : "v"(lo), "v"(hi)); return r; }
; #define SWAIT() asm volatile("s_waitcnt vmcnt(2)" ::: "memory")
; template <int DQK, bool FIXM> ...
;     ...
;     const bf16_t* Qw = Qp + (size_t)(wid * 32 + r32) * ldq + hi * 8;
; #pragma unroll
;     for (int d0 = 0; d0 < NQ; ++d0) qr[d0] = *(const bf16x8*)(Qw + d0 * 16);
;     if constexpr (DQK == 96) { if (qtok0 >= 0) {
;         const int t = qtok0 + wid * 32 + r32, gr = t >> 6, gc = t & 63;
; #pragma unroll
;         for (int e = 0; e < 2; ++e) { const f32x2* tp = (e == 0) ? rope + gr * 8 + hi * 4 : rope + 2048 + gc * 8 + hi * 4;
;             const f32x4 cs0 = *(const f32x4*)tp, cs1 = *(const f32x4*)(tp + 2);
;             const u32x4 w = __builtin_bit_cast(u32x4, qr[4 + e]); u32x4 o;
;             { const float x1 = bf16lo(w.x), x2 = bf16hi(w.x); o.x = cvt_pk_bf16(x1 * cs0[0] - x2 * cs0[1], x1 * cs0[1] + x2 * cs0[0]); }
;             { const float x1 = bf16lo(w.y), x2 = bf16hi(w.y); o.y = cvt_pk_bf16(x1 * cs0[2] - x2 * cs0[3], x1 * cs0[3] + x2 * cs0[2]); }
;             { const float x1 = bf16lo(w.z), x2 = bf16hi(w.z); o.z = cvt_pk_bf16(x1 * cs1[0] - x2 * cs1[1], x1 * cs1[1] + x2 * cs1[0]); }
;             { const float x1 = bf16lo(w.w), x2 = bf16hi(w.w); o.w = cvt_pk_bf16(x1 * cs1[2] - x2 * cs1[3], x1 * cs1[3] + x2 * cs1[2]); }
;             qr[4 + e] = __builtin_bit_cast(bf16x8, o); } } }
;     const int sr = tid >> 3, c8 = tid & 7, sr2 = (tid >> 2) & 63, c4 = tid & 3;
;     const bool krw = (DQK == 96) && (tid < 256);
;     const int kn_st = B_KN + swz64(sr, c8), v_stw = B_V + v_st(sr, c8 * 8), kr_st = B_KR + swz32(sr2, c4);
;     const unsigned vb0 = (unsigned)(uintptr_t)lds + B_V + v_rd_base(lane);
;     bf16x8 skn[2], sv[2], skr[2];
;     ...
;     f32x16 pA0, pA1, pB0, pB1; float alA, alB; bf16x8 pa0, pa1, pa2, pa3;
;     int bV = 0, bK = BUF, bW = 2 * BUF;
;     ...
;     __syncthreads();
;     SLOAD(0, 0); asm volatile("s_waitcnt vmcnt(0)" ::: "memory"); SWRITE(0, 0);
;     SLOAD(1, 1); if (2 < NT) SLOAD(0, 2);
;     __syncthreads();
;     qkt<DQK>(pA0, pA1, lds, qr, r32, hi, negm);
;     if (FIXM) { alA = 1.f; _Pragma("unroll") for (int r = 0; r < 16; ++r) pA0[r] = __builtin_amdgcn_exp2f(pA0[r]); } else partialSM<true>(pA0, pA1, m_reg, negm, alA);
;     SWAIT(); SWRITEO(BUF, 1);
.LBB0_496:
	s_lshr_b32 s8, s8, 6
	s_and_b64 s[0:1], s[10:11], exec
	s_cselect_b32 s8, s8, s14
	s_and_b32 s9, s8, 7
	s_lshl_b64 s[0:1], s[4:5], 10
	s_add_u32 s0, s15, s0
	s_addc_u32 s1, s16, s1
	s_lshl_b32 s34, s9, 6
	s_lshl_b32 s9, s9, 7
	s_add_u32 s38, s0, s9
	s_addc_u32 s39, s1, 0
	s_lshl_b32 s0, s8, 5
	s_and_b32 s8, s0, 0x80
	s_add_u32 s0, s19, s8
	v_add_u32_e32 v16, s36, v1
	s_addc_u32 s1, s20, 0
	v_ashrrev_i32_e32 v17, 31, v16
	s_add_u32 s8, s23, s8
	v_lshl_add_u64 v[4:5], s[38:39], 0, v[192:193]
	v_lshlrev_b32_e32 v2, 1, v200
	v_lshlrev_b64 v[16:17], 8, v[16:17]
	s_addc_u32 s9, s24, 0
	v_lshl_add_u64 v[4:5], v[4:5], 0, v[2:3]
	v_lshl_add_u64 v[34:35], s[0:1], 0, v[16:17]
	v_lshlrev_b32_e32 v2, 1, v188
	v_lshl_add_u64 v[34:35], v[34:35], 0, v[2:3]
	v_lshl_add_u64 v[16:17], s[8:9], 0, v[16:17]
	global_load_dwordx4 v[114:117], v[4:5], off
	global_load_dwordx4 v[12:15], v[4:5], off offset:32
	global_load_dwordx4 v[8:11], v[4:5], off offset:64
	s_nop 0
	global_load_dwordx4 v[4:7], v[4:5], off offset:96
	s_barrier
	v_lshl_add_u64 v[16:17], v[16:17], 0, v[2:3]
	global_load_dwordx4 v[34:37], v[34:35], off
	s_nop 0
	global_load_dwordx4 v[38:41], v[16:17], off
	s_lshl_b32 s36, s31, 6
	s_sub_i32 s36, s29, s36
	s_and_b64 s[10:11], s[10:11], exec
	s_cselect_b32 s10, s12, s36
	v_add_u32_e32 v16, s10, v191
	v_ashrrev_i32_e32 v17, 31, v16
	v_lshlrev_b64 v[16:17], 8, v[16:17]
	v_add_u32_e32 v42, s10, v189
	v_lshl_add_u64 v[44:45], s[0:1], 0, v[16:17]
	v_lshl_add_u64 v[16:17], s[8:9], 0, v[16:17]
	s_waitcnt vmcnt(0)
	v_lshl_add_u64 v[44:45], v[44:45], 0, v[2:3]
	v_lshl_add_u64 v[16:17], v[16:17], 0, v[2:3]
	v_ashrrev_i32_e32 v43, 31, v42
	global_load_dwordx4 v[58:61], v[44:45], off
	global_load_dwordx4 v[62:65], v[16:17], off
	v_lshlrev_b64 v[16:17], 8, v[42:43]
	v_lshl_add_u64 v[42:43], s[0:1], 0, v[16:17]
	v_lshl_add_u64 v[16:17], s[8:9], 0, v[16:17]
	v_lshl_add_u64 v[42:43], v[42:43], 0, v[2:3]
	v_lshl_add_u64 v[16:17], v[16:17], 0, v[2:3]
	global_load_dwordx4 v[118:121], v[42:43], off
	global_load_dwordx4 v[122:125], v[16:17], off
	v_add_u32_e32 v106, 0, v187
	v_add_u32_e32 v46, v208, v209
	v_add_u32_e32 v107, 0, v214
	v_add_u32_e32 v16, v208, v210
	v_add_u32_e32 v17, v208, v211
	v_add_u32_e32 v57, v208, v212
	v_mov_b32_e32 v136, 0
	s_mov_b32 s10, 0xa000
	s_movk_i32 s11, 0x5000
	v_mov_b32_e32 v137, v221
	v_mov_b32_e32 v50, 0
	v_mov_b32_e32 v42, v136
	v_mov_b32_e32 v43, v136
	v_mov_b32_e32 v48, v136
	v_mov_b32_e32 v49, v136
	v_mov_b32_e32 v51, v136
	v_mov_b32_e32 v56, v136
	v_lshl_add_u64 v[134:135], s[8:9], 0, v[2:3]
	s_mov_b64 s[44:45], s[8:9]
	s_waitcnt vmcnt(5)
	ds_write_b128 v106, v[34:37]
	s_waitcnt vmcnt(4)
	ds_write_b128 v107, v[38:41] offset:12288
	s_waitcnt lgkmcnt(0)
	s_barrier
	ds_read_b128 v[34:37], v46
	ds_read_b128 v[38:41], v46 offset:4096
	s_waitcnt lgkmcnt(1)
	v_mfma_f32_32x32x16_bf16 v[82:97], v[34:37], v[114:117], v[18:33]
	ds_read_b128 v[34:37], v16
	ds_read_b128 v[44:47], v17
	ds_read_b128 v[52:55], v17 offset:4096
	ds_read_b128 v[98:101], v57
	ds_read_b128 v[102:105], v57 offset:4096
	v_mov_b32_e32 v57, v136
	s_waitcnt lgkmcnt(5)
	v_mfma_f32_32x32x16_bf16 v[66:81], v[38:41], v[114:117], v[18:33]
	ds_read_b128 v[38:41], v16 offset:4096
	s_waitcnt vmcnt(2)
	v_lshl_add_u64 v[16:17], s[0:1], 0, v[2:3]
	s_mov_b64 s[42:43], s[0:1]
	s_add_i32 s0, s30, -1
	s_waitcnt vmcnt(3)
	ds_write_b128 v106, v[58:61] offset:20480
	s_waitcnt vmcnt(2)
	ds_write_b128 v107, v[62:65] offset:32768
	v_mov_b32_e32 v58, v136
	v_mov_b32_e32 v59, v136
	s_waitcnt lgkmcnt(7)
	v_mfma_f32_32x32x16_bf16 v[82:97], v[34:37], v[12:15], v[82:97]
	v_mov_b32_e32 v34, 0
	v_mov_b32_e32 v35, v136
	v_mov_b32_e32 v36, v136
	v_mov_b32_e32 v37, v136
	v_mov_b32_e32 v60, v136
	v_mov_b32_e32 v61, v136
	v_mov_b32_e32 v62, v136
	s_waitcnt lgkmcnt(2)
	v_mfma_f32_32x32x16_bf16 v[66:81], v[38:41], v[12:15], v[66:81]
	v_mov_b32_e32 v38, v136
	v_mov_b32_e32 v39, v136
	v_mov_b32_e32 v40, v136
	v_mov_b32_e32 v41, v136
	v_mov_b32_e32 v63, v136
	v_mov_b32_e32 v64, v136
	v_mov_b32_e32 v65, v136
	v_mfma_f32_32x32x16_bf16 v[82:97], v[44:47], v[8:11], v[82:97]
	v_mov_b32_e32 v44, v136
	v_mov_b32_e32 v45, v136
	v_mov_b32_e32 v46, v136
	v_mov_b32_e32 v47, v136
	v_mfma_f32_32x32x16_bf16 v[66:81], v[52:55], v[8:11], v[66:81]
	v_mov_b32_e32 v52, v136
	v_mov_b32_e32 v53, v136
	v_mov_b32_e32 v54, v136
	v_mov_b32_e32 v55, v136
	v_mfma_f32_32x32x16_bf16 v[82:97], v[98:101], v[4:7], v[82:97]
	v_mfma_f32_32x32x16_bf16 v[66:81], v[102:105], v[4:7], v[66:81]
	s_nop 10
	v_exp_f32_e32 v143, v82
	v_exp_f32_e32 v145, v83
	v_exp_f32_e32 v141, v84
	v_exp_f32_e32 v144, v85
	v_exp_f32_e32 v139, v86
	v_exp_f32_e32 v142, v87
	v_exp_f32_e32 v138, v88
	v_exp_f32_e32 v140, v89
	v_exp_f32_e32 v151, v90
	v_exp_f32_e32 v153, v91
	v_exp_f32_e32 v149, v92
	v_exp_f32_e32 v152, v93
	v_exp_f32_e32 v147, v94
	v_exp_f32_e32 v150, v95
	v_exp_f32_e32 v146, v96
	v_exp_f32_e32 v148, v97
	v_add_u32_e32 v223, v208, v209
	v_add_u32_e32 v252, v208, v210
	v_add_u32_e32 v253, v208, v211
	v_add_u32_e32 v2, v208, v212
; #define LAS __attribute__((address_space(3)))
; __device__ __forceinline__ void finishSM(f32x16& p0, f32x16& p1, float alpha, float& l_reg, bf16x8& pa0, bf16x8& pa1, bf16x8& pa2, bf16x8& pa3) {
; #pragma unroll
;     for (int r = 0; r < 16; ++r) p1[r] = EXP_PROBE ? fmaf(p1[r], 0.001f, 1.f) : __builtin_amdgcn_exp2f(p1[r]);
;     float ps = 0.f;
; #pragma unroll
;     for (int r = 0; r < 16; ++r) ps += p0[r];
; #pragma unroll
;     for (int r = 0; r < 16; ++r) ps += p1[r];
;     { auto rr = __builtin_amdgcn_permlane32_swap(__float_as_uint(ps), __float_as_uint(ps), false, false);
;       ps = __uint_as_float(rr[0]) + __uint_as_float(rr[1]); }
;     l_reg = l_reg * alpha + ps;
;     ATT_PKN(p0, 0, pa0); ATT_PKN(p0, 8, pa1); ATT_PKN(p1, 0, pa2); ATT_PKN(p1, 8, pa3);
; }
; template <int DQK> __device__ __forceinline__ void qkt(f32x16& p0, f32x16& p1, const LAS char* buf, const bf16x8* qr, int r32, int hi, const f32x16& negm) {
; #pragma unroll
;     for (int d0 = 0; d0 < 4; ++d0) { const int ch = d0 * 2 + hi;
;         const bf16x8 b0 = *(const LAS bf16x8*)(buf + B_KN + swz64(r32, ch));
;         const bf16x8 b1 = *(const LAS bf16x8*)(buf + B_KN + swz64(32 + r32, ch));
;         p0 = __builtin_amdgcn_mfma_f32_32x32x16_bf16(b0, qr[d0], d0 == 0 ? negm : p0, 0, 0, 0);
;         p1 = __builtin_amdgcn_mfma_f32_32x32x16_bf16(b1, qr[d0], d0 == 0 ? negm : p1, 0, 0, 0); }
; template <bool FIXM> __device__ __forceinline__ void pv_psm(f32x16& o0, f32x16& o1, unsigned vb, bf16x8 pa0, bf16x8 pa1, bf16x8 pa2, bf16x8 pa3,
;                                        f32x16& p0, f32x16& p1, float& m_reg, f32x16& negm, float& alpha) {
;     { const s16x4 l0 = tr_read<v_rd_off(0, 0, 0)>(vb), h0 = tr_read<v_rd_off(0, 0, 1)>(vb), l1 = tr_read<v_rd_off(0, 1, 0)>(vb), h1 = tr_read<v_rd_off(0, 1, 1)>(vb);
;       const s16x4 l2 = tr_read<v_rd_off(0, 2, 0)>(vb), h2 = tr_read<v_rd_off(0, 2, 1)>(vb), l3 = tr_read<v_rd_off(0, 3, 0)>(vb), h3 = tr_read<v_rd_off(0, 3, 1)>(vb);
;       float pmax = 0.f; SBAR(); if (!FIXM) pmax = psm_max(p0, p1); else { _Pragma("unroll") for (int r = 0; r < 8; ++r) p0[r] = __builtin_amdgcn_exp2f(p0[r]); } SBAR();
;       asm volatile("s_waitcnt lgkmcnt(0)" ::: "memory"); SBAR();
;       o0 = __builtin_amdgcn_mfma_f32_32x32x16_bf16(ATT_PK(l0, h0), pa0, o0, 0, 0, 0);
;       o0 = __builtin_amdgcn_mfma_f32_32x32x16_bf16(ATT_PK(l1, h1), pa1, o0, 0, 0, 0);
.LBB0_497:
	s_waitcnt lgkmcnt(0)
	s_barrier
	ds_read_b128 v[224:227], v223 offset:20480
	ds_read_b128 v[228:231], v223 offset:24576
	ds_read_b128 v[232:235], v252 offset:20480
	ds_read_b128 v[236:239], v252 offset:24576
	ds_read_b128 v[240:243], v253 offset:20480
	ds_read_b128 v[244:247], v253 offset:24576
	ds_read_b128 v[248:251], v2 offset:20480
	v_exp_f32_e32 v66, v66
	v_exp_f32_e32 v67, v67
	v_exp_f32_e32 v68, v68
	v_exp_f32_e32 v69, v69
	v_exp_f32_e32 v70, v70
	v_exp_f32_e32 v71, v71
	v_exp_f32_e32 v72, v72
	v_exp_f32_e32 v73, v73
	s_waitcnt lgkmcnt(6)
	v_mfma_f32_32x32x16_bf16 v[98:113], v[224:227], v[114:117], v[18:33]
	ds_read_b128 v[224:227], v2 offset:24576
	v_exp_f32_e32 v74, v74
	v_exp_f32_e32 v75, v75
	v_exp_f32_e32 v76, v76
	v_cvt_pk_bf16_f32 v156, v143, v145
	v_cvt_pk_bf16_f32 v157, v141, v144
	v_add_f32_e32 v164, 0, v143
	v_add_f32_e32 v164, v145, v164
	v_add_f32_e32 v164, v141, v164
	s_waitcnt lgkmcnt(6)
	v_mfma_f32_32x32x16_bf16 v[82:97], v[228:231], v[114:117], v[18:33]
	v_exp_f32_e32 v77, v77
	v_exp_f32_e32 v78, v78
	v_exp_f32_e32 v79, v79
	v_cvt_pk_bf16_f32 v158, v139, v142
	v_cvt_pk_bf16_f32 v159, v138, v140
	v_add_f32_e32 v164, v144, v164
	v_add_f32_e32 v164, v139, v164
	v_add_f32_e32 v164, v142, v164
	s_waitcnt lgkmcnt(5)
	v_mfma_f32_32x32x16_bf16 v[98:113], v[232:235], v[12:15], v[98:113]
	v_exp_f32_e32 v80, v80
	v_exp_f32_e32 v81, v81
	v_cvt_pk_bf16_f32 v160, v151, v153
	v_cvt_pk_bf16_f32 v161, v149, v152
	v_cvt_pk_bf16_f32 v162, v147, v150
	v_cvt_pk_bf16_f32 v163, v146, v148
	v_add_f32_e32 v164, v138, v164
	v_add_f32_e32 v164, v140, v164
	v_add_f32_e32 v164, v151, v164
	s_waitcnt lgkmcnt(4)
	v_mfma_f32_32x32x16_bf16 v[82:97], v[236:239], v[12:15], v[82:97]
	v_add_f32_e32 v164, v153, v164
	v_add_f32_e32 v164, v149, v164
	v_add_f32_e32 v164, v152, v164
	v_add_f32_e32 v164, v147, v164
	v_add_f32_e32 v164, v150, v164
	v_add_f32_e32 v164, v146, v164
	v_add_f32_e32 v164, v148, v164
	s_waitcnt lgkmcnt(3)
	v_mfma_f32_32x32x16_bf16 v[98:113], v[240:243], v[8:11], v[98:113]
	ds_read_b64_tr_b16 v[138:139], v213 offset:0
	ds_read_b64_tr_b16 v[140:141], v213 offset:1024
	ds_read_b64_tr_b16 v[142:143], v213 offset:2048
	ds_read_b64_tr_b16 v[144:145], v213 offset:3072
	v_add_f32_e32 v164, v66, v164
	v_add_f32_e32 v164, v67, v164
	v_add_f32_e32 v164, v68, v164
	v_add_f32_e32 v164, v69, v164
	s_waitcnt lgkmcnt(6)
	v_mfma_f32_32x32x16_bf16 v[82:97], v[244:247], v[8:11], v[82:97]
	ds_read_b64_tr_b16 v[146:147], v213 offset:4096
	ds_read_b64_tr_b16 v[148:149], v213 offset:5120
	ds_read_b64_tr_b16 v[150:151], v213 offset:6144
	ds_read_b64_tr_b16 v[152:153], v213 offset:7168
	v_add_f32_e32 v164, v70, v164
	v_add_f32_e32 v164, v71, v164
	v_add_f32_e32 v164, v72, v164
	v_add_f32_e32 v164, v73, v164
	s_waitcnt lgkmcnt(9)
	v_mfma_f32_32x32x16_bf16 v[98:113], v[248:251], v[4:7], v[98:113]
	v_add_f32_e32 v164, v74, v164
	v_add_f32_e32 v164, v75, v164
	v_add_f32_e32 v164, v76, v164
	v_add_f32_e32 v164, v77, v164
	s_waitcnt lgkmcnt(8)
	v_mfma_f32_32x32x16_bf16 v[82:97], v[224:227], v[4:7], v[82:97]
	ds_read_b64_tr_b16 v[224:225], v213 offset:512
	ds_read_b64_tr_b16 v[226:227], v213 offset:1536
	ds_read_b64_tr_b16 v[228:229], v213 offset:2560
	ds_read_b64_tr_b16 v[230:231], v213 offset:3584
	ds_read_b64_tr_b16 v[232:233], v213 offset:4608
	ds_read_b64_tr_b16 v[234:235], v213 offset:5632
	ds_read_b64_tr_b16 v[236:237], v213 offset:6656
	ds_read_b64_tr_b16 v[238:239], v213 offset:7680
	s_waitcnt lgkmcnt(8)
	v_mfma_f32_32x32x16_bf16 v[50:65], v[138:141], v[156:159], v[50:65]
	v_add_f32_e32 v164, v78, v164
	v_add_f32_e32 v164, v79, v164
	v_add_f32_e32 v164, v80, v164
	v_add_f32_e32 v154, v81, v164
	v_mov_b32_e32 v155, v154
	v_mfma_f32_32x32x16_bf16 v[50:65], v[142:145], v[160:163], v[50:65]
	v_cvt_pk_bf16_f32 v66, v66, v67
	v_cvt_pk_bf16_f32 v67, v68, v69
	v_cvt_pk_bf16_f32 v68, v70, v71
	v_cvt_pk_bf16_f32 v69, v72, v73
	v_cvt_pk_bf16_f32 v70, v74, v75
	v_cvt_pk_bf16_f32 v71, v76, v77
	v_cvt_pk_bf16_f32 v72, v78, v79
	v_cvt_pk_bf16_f32 v73, v80, v81
	v_permlane32_swap_b32_e32 v154, v155
	v_mfma_f32_32x32x16_bf16 v[50:65], v[146:149], v[66:69], v[50:65]
	s_add_i32 s8, s13, -1
	s_cmp_lt_u32 s8, s31
	s_cselect_b32 s9, 0, s31
	s_cselect_b32 s35, s12, s29
	s_lshl_b32 s9, s9, 6
	s_sub_i32 s9, s35, s9
	v_add_u32_e32 v126, s9, v137
	v_subrev_u32_e32 v126, 64, v126
	v_ashrrev_i32_e32 v127, 31, v126
	v_mfma_f32_32x32x16_bf16 v[50:65], v[150:153], v[70:73], v[50:65]
	v_lshlrev_b64 v[126:127], 8, v[126:127]
	v_lshl_add_u64 v[128:129], v[16:17], 0, v[126:127]
	v_lshl_add_u64 v[126:127], v[134:135], 0, v[126:127]
	global_load_dwordx4 v[130:133], v[128:129], off
	s_nop 0
	global_load_dwordx4 v[126:129], v[126:127], off
	s_waitcnt lgkmcnt(0)
	v_mfma_f32_32x32x16_bf16 v[34:49], v[224:227], v[156:159], v[34:49]
	s_waitcnt vmcnt(2)
	ds_write_b128 v187, v[118:121] offset:40960
	ds_write_b128 v214, v[122:125] offset:53248
	v_exp_f32_e32 v168, v98
	v_exp_f32_e32 v169, v99
	v_mfma_f32_32x32x16_bf16 v[34:49], v[228:231], v[160:163], v[34:49]
	v_exp_f32_e32 v170, v100
	v_exp_f32_e32 v171, v101
	v_exp_f32_e32 v172, v102
	v_exp_f32_e32 v173, v103
	v_mfma_f32_32x32x16_bf16 v[34:49], v[232:235], v[66:69], v[34:49]
	v_exp_f32_e32 v174, v104
	v_exp_f32_e32 v175, v105
	v_exp_f32_e32 v176, v106
	v_exp_f32_e32 v177, v107
	v_exp_f32_e32 v178, v108
	v_mfma_f32_32x32x16_bf16 v[34:49], v[236:239], v[70:73], v[34:49]
	v_exp_f32_e32 v179, v109
	v_exp_f32_e32 v180, v110
	v_exp_f32_e32 v181, v111
	v_exp_f32_e32 v182, v112
	v_exp_f32_e32 v183, v113
	s_waitcnt lgkmcnt(0)
	s_barrier
; #define LAS __attribute__((address_space(3)))
; __device__ __forceinline__ void finishSM(f32x16& p0, f32x16& p1, float alpha, float& l_reg, bf16x8& pa0, bf16x8& pa1, bf16x8& pa2, bf16x8& pa3) {
; #pragma unroll
;     for (int r = 0; r < 16; ++r) p1[r] = EXP_PROBE ? fmaf(p1[r], 0.001f, 1.f) : __builtin_amdgcn_exp2f(p1[r]);
;     float ps = 0.f;
; #pragma unroll
;     for (int r = 0; r < 16; ++r) ps += p0[r];
; #pragma unroll
;     for (int r = 0; r < 16; ++r) ps += p1[r];
;     { auto rr = __builtin_amdgcn_permlane32_swap(__float_as_uint(ps), __float_as_uint(ps), false, false);
;       ps = __uint_as_float(rr[0]) + __uint_as_float(rr[1]); }
;     l_reg = l_reg * alpha + ps;
;     ATT_PKN(p0, 0, pa0); ATT_PKN(p0, 8, pa1); ATT_PKN(p1, 0, pa2); ATT_PKN(p1, 8, pa3);
; }
; template <int DQK> __device__ __forceinline__ void qkt(f32x16& p0, f32x16& p1, const LAS char* buf, const bf16x8* qr, int r32, int hi, const f32x16& negm) {
; #pragma unroll
;     for (int d0 = 0; d0 < 4; ++d0) { const int ch = d0 * 2 + hi;
;         const bf16x8 b0 = *(const LAS bf16x8*)(buf + B_KN + swz64(r32, ch));
;         const bf16x8 b1 = *(const LAS bf16x8*)(buf + B_KN + swz64(32 + r32, ch));
;         p0 = __builtin_amdgcn_mfma_f32_32x32x16_bf16(b0, qr[d0], d0 == 0 ? negm : p0, 0, 0, 0);
;         p1 = __builtin_amdgcn_mfma_f32_32x32x16_bf16(b1, qr[d0], d0 == 0 ? negm : p1, 0, 0, 0); }
; template <bool FIXM> __device__ __forceinline__ void pv_psm(f32x16& o0, f32x16& o1, unsigned vb, bf16x8 pa0, bf16x8 pa1, bf16x8 pa2, bf16x8 pa3,
;                                        f32x16& p0, f32x16& p1, float& m_reg, f32x16& negm, float& alpha) {
;     { const s16x4 l0 = tr_read<v_rd_off(0, 0, 0)>(vb), h0 = tr_read<v_rd_off(0, 0, 1)>(vb), l1 = tr_read<v_rd_off(0, 1, 0)>(vb), h1 = tr_read<v_rd_off(0, 1, 1)>(vb);
;       const s16x4 l2 = tr_read<v_rd_off(0, 2, 0)>(vb), h2 = tr_read<v_rd_off(0, 2, 1)>(vb), l3 = tr_read<v_rd_off(0, 3, 0)>(vb), h3 = tr_read<v_rd_off(0, 3, 1)>(vb);
;       float pmax = 0.f; SBAR(); if (!FIXM) pmax = psm_max(p0, p1); else { _Pragma("unroll") for (int r = 0; r < 8; ++r) p0[r] = __builtin_amdgcn_exp2f(p0[r]); } SBAR();
;       asm volatile("s_waitcnt lgkmcnt(0)" ::: "memory"); SBAR();
;       o0 = __builtin_amdgcn_mfma_f32_32x32x16_bf16(ATT_PK(l0, h0), pa0, o0, 0, 0, 0);
;       o0 = __builtin_amdgcn_mfma_f32_32x32x16_bf16(ATT_PK(l1, h1), pa1, o0, 0, 0, 0);
	ds_read_b128 v[224:227], v223 offset:40960
	ds_read_b128 v[228:231], v223 offset:45056
	ds_read_b128 v[232:235], v252 offset:40960
	ds_read_b128 v[236:239], v252 offset:45056
	ds_read_b128 v[240:243], v253 offset:40960
	ds_read_b128 v[244:247], v253 offset:45056
	ds_read_b128 v[248:251], v2 offset:40960
	v_exp_f32_e32 v82, v82
	v_exp_f32_e32 v83, v83
	v_exp_f32_e32 v84, v84
	v_exp_f32_e32 v85, v85
	v_exp_f32_e32 v86, v86
	v_exp_f32_e32 v87, v87
	v_exp_f32_e32 v88, v88
	v_exp_f32_e32 v89, v89
	s_waitcnt lgkmcnt(6)
	v_mfma_f32_32x32x16_bf16 v[98:113], v[224:227], v[114:117], v[18:33]
	ds_read_b128 v[224:227], v2 offset:45056
	v_exp_f32_e32 v90, v90
	v_exp_f32_e32 v91, v91
	v_exp_f32_e32 v92, v92
	v_cvt_pk_bf16_f32 v156, v168, v169
	v_cvt_pk_bf16_f32 v157, v170, v171
	v_add_f32_e32 v164, 0, v168
	v_add_f32_e32 v164, v169, v164
	v_add_f32_e32 v164, v170, v164
	s_waitcnt lgkmcnt(6)
	v_mfma_f32_32x32x16_bf16 v[66:81], v[228:231], v[114:117], v[18:33]
	v_exp_f32_e32 v93, v93
	v_exp_f32_e32 v94, v94
	v_exp_f32_e32 v95, v95
	v_cvt_pk_bf16_f32 v158, v172, v173
	v_cvt_pk_bf16_f32 v159, v174, v175
	v_add_f32_e32 v164, v171, v164
	v_add_f32_e32 v164, v172, v164
	v_add_f32_e32 v164, v173, v164
	s_waitcnt lgkmcnt(5)
	v_mfma_f32_32x32x16_bf16 v[98:113], v[232:235], v[12:15], v[98:113]
	v_exp_f32_e32 v96, v96
	v_exp_f32_e32 v97, v97
	v_cvt_pk_bf16_f32 v160, v176, v177
	v_cvt_pk_bf16_f32 v161, v178, v179
	v_cvt_pk_bf16_f32 v162, v180, v181
	v_cvt_pk_bf16_f32 v163, v182, v183
	v_add_f32_e32 v164, v174, v164
	v_add_f32_e32 v164, v175, v164
	v_add_f32_e32 v164, v176, v164
	s_waitcnt lgkmcnt(4)
	v_mfma_f32_32x32x16_bf16 v[66:81], v[236:239], v[12:15], v[66:81]
	v_add_f32_e32 v164, v177, v164
	v_add_f32_e32 v164, v178, v164
	v_add_f32_e32 v164, v179, v164
	v_add_f32_e32 v164, v180, v164
	v_add_f32_e32 v164, v181, v164
	v_add_f32_e32 v164, v182, v164
	v_add_f32_e32 v164, v183, v164
	s_waitcnt lgkmcnt(3)
	v_mfma_f32_32x32x16_bf16 v[98:113], v[240:243], v[8:11], v[98:113]
	ds_read_b64_tr_b16 v[168:169], v213 offset:20480
	ds_read_b64_tr_b16 v[170:171], v213 offset:21504
	ds_read_b64_tr_b16 v[172:173], v213 offset:22528
	ds_read_b64_tr_b16 v[174:175], v213 offset:23552
	v_add_f32_e32 v164, v82, v164
	v_add_f32_e32 v164, v83, v164
	v_add_f32_e32 v164, v84, v164
	v_add_f32_e32 v164, v85, v164
	s_waitcnt lgkmcnt(6)
	v_mfma_f32_32x32x16_bf16 v[66:81], v[244:247], v[8:11], v[66:81]
	ds_read_b64_tr_b16 v[176:177], v213 offset:24576
	ds_read_b64_tr_b16 v[178:179], v213 offset:25600
	ds_read_b64_tr_b16 v[180:181], v213 offset:26624
	ds_read_b64_tr_b16 v[182:183], v213 offset:27648
	v_add_f32_e32 v164, v86, v164
	v_add_f32_e32 v164, v87, v164
	v_add_f32_e32 v164, v88, v164
	v_add_f32_e32 v164, v89, v164
	s_waitcnt lgkmcnt(9)
	v_mfma_f32_32x32x16_bf16 v[98:113], v[248:251], v[4:7], v[98:113]
	v_add_f32_e32 v164, v90, v164
	v_add_f32_e32 v164, v91, v164
	v_add_f32_e32 v164, v92, v164
	v_add_f32_e32 v164, v93, v164
	s_waitcnt lgkmcnt(8)
	v_mfma_f32_32x32x16_bf16 v[66:81], v[224:227], v[4:7], v[66:81]
	ds_read_b64_tr_b16 v[224:225], v213 offset:20992
	ds_read_b64_tr_b16 v[226:227], v213 offset:22016
	ds_read_b64_tr_b16 v[228:229], v213 offset:23040
	ds_read_b64_tr_b16 v[230:231], v213 offset:24064
	ds_read_b64_tr_b16 v[232:233], v213 offset:25088
	ds_read_b64_tr_b16 v[234:235], v213 offset:26112
	ds_read_b64_tr_b16 v[236:237], v213 offset:27136
	ds_read_b64_tr_b16 v[238:239], v213 offset:28160
	s_waitcnt lgkmcnt(8)
	v_mfma_f32_32x32x16_bf16 v[50:65], v[168:171], v[156:159], v[50:65]
	v_add_f32_e32 v164, v94, v164
	v_add_f32_e32 v164, v95, v164
	v_add_f32_e32 v164, v96, v164
	v_add_f32_e32 v164, v97, v164
	v_mov_b32_e32 v165, v164
	v_mfma_f32_32x32x16_bf16 v[50:65], v[172:175], v[160:163], v[50:65]
	v_cvt_pk_bf16_f32 v82, v82, v83
	v_cvt_pk_bf16_f32 v83, v84, v85
	v_cvt_pk_bf16_f32 v84, v86, v87
	v_cvt_pk_bf16_f32 v85, v88, v89
	v_cvt_pk_bf16_f32 v86, v90, v91
	v_cvt_pk_bf16_f32 v87, v92, v93
	v_cvt_pk_bf16_f32 v88, v94, v95
	v_cvt_pk_bf16_f32 v89, v96, v97
	v_permlane32_swap_b32_e32 v164, v165
	v_mfma_f32_32x32x16_bf16 v[50:65], v[176:179], v[82:85], v[50:65]
	v_mfma_f32_32x32x16_bf16 v[50:65], v[180:183], v[86:89], v[50:65]
	s_cmp_ge_u32 s13, s30
	s_cbranch_scc1 .Lgqa_b_noload_0
	s_cmp_lt_u32 s13, s31
	s_cselect_b32 s9, 0, s31
	s_cselect_b32 s35, s12, s29
	s_lshl_b32 s9, s9, 6
	s_sub_i32 s9, s35, s9
	v_add_u32_e32 v118, s9, v137
	v_ashrrev_i32_e32 v119, 31, v118
	v_lshlrev_b64 v[118:119], 8, v[118:119]
	v_lshl_add_u64 v[120:121], v[16:17], 0, v[118:119]
	v_lshl_add_u64 v[122:123], v[134:135], 0, v[118:119]
	global_load_dwordx4 v[118:121], v[120:121], off
	s_nop 0
	global_load_dwordx4 v[122:125], v[122:123], off
; #define LAS __attribute__((address_space(3)))
; __device__ __forceinline__ void finishSM(f32x16& p0, f32x16& p1, float alpha, float& l_reg, bf16x8& pa0, bf16x8& pa1, bf16x8& pa2, bf16x8& pa3) {
; #pragma unroll
;     for (int r = 0; r < 16; ++r) p1[r] = EXP_PROBE ? fmaf(p1[r], 0.001f, 1.f) : __builtin_amdgcn_exp2f(p1[r]);
;     float ps = 0.f;
; #pragma unroll
;     for (int r = 0; r < 16; ++r) ps += p0[r];
; #pragma unroll
;     for (int r = 0; r < 16; ++r) ps += p1[r];
;     { auto rr = __builtin_amdgcn_permlane32_swap(__float_as_uint(ps), __float_as_uint(ps), false, false);
;       ps = __uint_as_float(rr[0]) + __uint_as_float(rr[1]); }
;     l_reg = l_reg * alpha + ps;
;     ATT_PKN(p0, 0, pa0); ATT_PKN(p0, 8, pa1); ATT_PKN(p1, 0, pa2); ATT_PKN(p1, 8, pa3);
; }
; template <int DQK> __device__ __forceinline__ void qkt(f32x16& p0, f32x16& p1, const LAS char* buf, const bf16x8* qr, int r32, int hi, const f32x16& negm) {
; #pragma unroll
;     for (int d0 = 0; d0 < 4; ++d0) { const int ch = d0 * 2 + hi;
;         const bf16x8 b0 = *(const LAS bf16x8*)(buf + B_KN + swz64(r32, ch));
;         const bf16x8 b1 = *(const LAS bf16x8*)(buf + B_KN + swz64(32 + r32, ch));
;         p0 = __builtin_amdgcn_mfma_f32_32x32x16_bf16(b0, qr[d0], d0 == 0 ? negm : p0, 0, 0, 0);
;         p1 = __builtin_amdgcn_mfma_f32_32x32x16_bf16(b1, qr[d0], d0 == 0 ? negm : p1, 0, 0, 0); }
; template <bool FIXM> __device__ __forceinline__ void pv_psm(f32x16& o0, f32x16& o1, unsigned vb, bf16x8 pa0, bf16x8 pa1, bf16x8 pa2, bf16x8 pa3,
;                                        f32x16& p0, f32x16& p1, float& m_reg, f32x16& negm, float& alpha) {
;     { const s16x4 l0 = tr_read<v_rd_off(0, 0, 0)>(vb), h0 = tr_read<v_rd_off(0, 0, 1)>(vb), l1 = tr_read<v_rd_off(0, 1, 0)>(vb), h1 = tr_read<v_rd_off(0, 1, 1)>(vb);
;       const s16x4 l2 = tr_read<v_rd_off(0, 2, 0)>(vb), h2 = tr_read<v_rd_off(0, 2, 1)>(vb), l3 = tr_read<v_rd_off(0, 3, 0)>(vb), h3 = tr_read<v_rd_off(0, 3, 1)>(vb);
;       float pmax = 0.f; SBAR(); if (!FIXM) pmax = psm_max(p0, p1); else { _Pragma("unroll") for (int r = 0; r < 8; ++r) p0[r] = __builtin_amdgcn_exp2f(p0[r]); } SBAR();
;       asm volatile("s_waitcnt lgkmcnt(0)" ::: "memory"); SBAR();
;       o0 = __builtin_amdgcn_mfma_f32_32x32x16_bf16(ATT_PK(l0, h0), pa0, o0, 0, 0, 0);
;       o0 = __builtin_amdgcn_mfma_f32_32x32x16_bf16(ATT_PK(l1, h1), pa1, o0, 0, 0, 0);
.Lgqa_b_ld_done_0:
	s_waitcnt lgkmcnt(0)
	v_mfma_f32_32x32x16_bf16 v[34:49], v[224:227], v[156:159], v[34:49]
	s_waitcnt vmcnt(2)
	ds_write_b128 v187, v[130:133] offset:0
	ds_write_b128 v214, v[126:129] offset:12288
	v_exp_f32_e32 v143, v98
	v_exp_f32_e32 v145, v99
	v_mfma_f32_32x32x16_bf16 v[34:49], v[228:231], v[160:163], v[34:49]
	v_exp_f32_e32 v141, v100
	v_exp_f32_e32 v144, v101
	v_exp_f32_e32 v139, v102
	v_exp_f32_e32 v142, v103
	v_mfma_f32_32x32x16_bf16 v[34:49], v[232:235], v[82:85], v[34:49]
	v_exp_f32_e32 v138, v104
	v_exp_f32_e32 v140, v105
	v_exp_f32_e32 v151, v106
	v_exp_f32_e32 v153, v107
	v_exp_f32_e32 v149, v108
	v_mfma_f32_32x32x16_bf16 v[34:49], v[236:239], v[86:89], v[34:49]
	v_exp_f32_e32 v152, v109
	v_exp_f32_e32 v147, v110
	v_exp_f32_e32 v150, v111
	v_exp_f32_e32 v146, v112
	v_exp_f32_e32 v148, v113
	v_add_f32_e32 v154, v154, v155
	v_add_f32_e32 v136, v136, v154
	v_add_f32_e32 v164, v164, v165
	v_add_f32_e32 v136, v136, v164
	s_add_i32 s13, s13, 2
	v_add_u32_e32 v137, 0x80, v137
	s_cmp_lt_u32 s8, s0
	s_cbranch_scc0 .Lgqa_exit_0
	s_waitcnt lgkmcnt(0)
	s_barrier
	ds_read_b128 v[224:227], v223 offset:0
	ds_read_b128 v[228:231], v223 offset:4096
	ds_read_b128 v[232:235], v252 offset:0
	ds_read_b128 v[236:239], v252 offset:4096
	ds_read_b128 v[240:243], v253 offset:0
	ds_read_b128 v[244:247], v253 offset:4096
	ds_read_b128 v[248:251], v2 offset:0
	v_exp_f32_e32 v66, v66
	v_exp_f32_e32 v67, v67
	v_exp_f32_e32 v68, v68
	v_exp_f32_e32 v69, v69
	v_exp_f32_e32 v70, v70
	v_exp_f32_e32 v71, v71
	v_exp_f32_e32 v72, v72
	v_exp_f32_e32 v73, v73
	s_waitcnt lgkmcnt(6)
	v_mfma_f32_32x32x16_bf16 v[98:113], v[224:227], v[114:117], v[18:33]
	ds_read_b128 v[224:227], v2 offset:4096
	v_exp_f32_e32 v74, v74
	v_exp_f32_e32 v75, v75
	v_exp_f32_e32 v76, v76
	v_cvt_pk_bf16_f32 v156, v143, v145
	v_cvt_pk_bf16_f32 v157, v141, v144
	v_add_f32_e32 v164, 0, v143
	v_add_f32_e32 v164, v145, v164
	v_add_f32_e32 v164, v141, v164
	s_waitcnt lgkmcnt(6)
	v_mfma_f32_32x32x16_bf16 v[82:97], v[228:231], v[114:117], v[18:33]
	v_exp_f32_e32 v77, v77
	v_exp_f32_e32 v78, v78
	v_exp_f32_e32 v79, v79
	v_cvt_pk_bf16_f32 v158, v139, v142
	v_cvt_pk_bf16_f32 v159, v138, v140
	v_add_f32_e32 v164, v144, v164
	v_add_f32_e32 v164, v139, v164
	v_add_f32_e32 v164, v142, v164
	s_waitcnt lgkmcnt(5)
	v_mfma_f32_32x32x16_bf16 v[98:113], v[232:235], v[12:15], v[98:113]
	v_exp_f32_e32 v80, v80
	v_exp_f32_e32 v81, v81
	v_cvt_pk_bf16_f32 v160, v151, v153
	v_cvt_pk_bf16_f32 v161, v149, v152
	v_cvt_pk_bf16_f32 v162, v147, v150
	v_cvt_pk_bf16_f32 v163, v146, v148
	v_add_f32_e32 v164, v138, v164
	v_add_f32_e32 v164, v140, v164
	v_add_f32_e32 v164, v151, v164
	s_waitcnt lgkmcnt(4)
	v_mfma_f32_32x32x16_bf16 v[82:97], v[236:239], v[12:15], v[82:97]
	v_add_f32_e32 v164, v153, v164
	v_add_f32_e32 v164, v149, v164
	v_add_f32_e32 v164, v152, v164
	v_add_f32_e32 v164, v147, v164
	v_add_f32_e32 v164, v150, v164
	v_add_f32_e32 v164, v146, v164
	v_add_f32_e32 v164, v148, v164
	s_waitcnt lgkmcnt(3)
	v_mfma_f32_32x32x16_bf16 v[98:113], v[240:243], v[8:11], v[98:113]
	ds_read_b64_tr_b16 v[138:139], v213 offset:40960
	ds_read_b64_tr_b16 v[140:141], v213 offset:41984
	ds_read_b64_tr_b16 v[142:143], v213 offset:43008
	ds_read_b64_tr_b16 v[144:145], v213 offset:44032
	v_add_f32_e32 v164, v66, v164
	v_add_f32_e32 v164, v67, v164
	v_add_f32_e32 v164, v68, v164
	v_add_f32_e32 v164, v69, v164
	s_waitcnt lgkmcnt(6)
	v_mfma_f32_32x32x16_bf16 v[82:97], v[244:247], v[8:11], v[82:97]
	ds_read_b64_tr_b16 v[146:147], v213 offset:45056
	ds_read_b64_tr_b16 v[148:149], v213 offset:46080
	ds_read_b64_tr_b16 v[150:151], v213 offset:47104
	ds_read_b64_tr_b16 v[152:153], v213 offset:48128
	v_add_f32_e32 v164, v70, v164
	v_add_f32_e32 v164, v71, v164
	v_add_f32_e32 v164, v72, v164
	v_add_f32_e32 v164, v73, v164
	s_waitcnt lgkmcnt(9)
	v_mfma_f32_32x32x16_bf16 v[98:113], v[248:251], v[4:7], v[98:113]
	v_add_f32_e32 v164, v74, v164
	v_add_f32_e32 v164, v75, v164
	v_add_f32_e32 v164, v76, v164
	v_add_f32_e32 v164, v77, v164
	s_waitcnt lgkmcnt(8)
	v_mfma_f32_32x32x16_bf16 v[82:97], v[224:227], v[4:7], v[82:97]
	ds_read_b64_tr_b16 v[224:225], v213 offset:41472
	ds_read_b64_tr_b16 v[226:227], v213 offset:42496
	ds_read_b64_tr_b16 v[228:229], v213 offset:43520
	ds_read_b64_tr_b16 v[230:231], v213 offset:44544
	ds_read_b64_tr_b16 v[232:233], v213 offset:45568
	ds_read_b64_tr_b16 v[234:235], v213 offset:46592
	ds_read_b64_tr_b16 v[236:237], v213 offset:47616
	ds_read_b64_tr_b16 v[238:239], v213 offset:48640
	s_waitcnt lgkmcnt(8)
	v_mfma_f32_32x32x16_bf16 v[50:65], v[138:141], v[156:159], v[50:65]
	v_add_f32_e32 v164, v78, v164
	v_add_f32_e32 v164, v79, v164
	v_add_f32_e32 v164, v80, v164
	v_add_f32_e32 v154, v81, v164
	v_mov_b32_e32 v155, v154
	v_mfma_f32_32x32x16_bf16 v[50:65], v[142:145], v[160:163], v[50:65]
	v_cvt_pk_bf16_f32 v66, v66, v67
	v_cvt_pk_bf16_f32 v67, v68, v69
	v_cvt_pk_bf16_f32 v68, v70, v71
	v_cvt_pk_bf16_f32 v69, v72, v73
	v_cvt_pk_bf16_f32 v70, v74, v75
	v_cvt_pk_bf16_f32 v71, v76, v77
	v_cvt_pk_bf16_f32 v72, v78, v79
	v_cvt_pk_bf16_f32 v73, v80, v81
	v_permlane32_swap_b32_e32 v154, v155
	v_mfma_f32_32x32x16_bf16 v[50:65], v[146:149], v[66:69], v[50:65]
	s_add_i32 s8, s13, -1
	s_cmp_lt_u32 s8, s31
	s_cselect_b32 s9, 0, s31
	s_cselect_b32 s35, s12, s29
	s_lshl_b32 s9, s9, 6
	s_sub_i32 s9, s35, s9
	v_add_u32_e32 v126, s9, v137
	v_subrev_u32_e32 v126, 64, v126
	v_ashrrev_i32_e32 v127, 31, v126
	v_mfma_f32_32x32x16_bf16 v[50:65], v[150:153], v[70:73], v[50:65]
	v_lshlrev_b64 v[126:127], 8, v[126:127]
	v_lshl_add_u64 v[128:129], v[16:17], 0, v[126:127]
	v_lshl_add_u64 v[126:127], v[134:135], 0, v[126:127]
	global_load_dwordx4 v[130:133], v[128:129], off
	s_nop 0
	global_load_dwordx4 v[126:129], v[126:127], off
	s_waitcnt lgkmcnt(0)
	v_mfma_f32_32x32x16_bf16 v[34:49], v[224:227], v[156:159], v[34:49]
	s_waitcnt vmcnt(2)
	ds_write_b128 v187, v[118:121] offset:20480
	ds_write_b128 v214, v[122:125] offset:32768
	v_exp_f32_e32 v168, v98
	v_exp_f32_e32 v169, v99
	v_mfma_f32_32x32x16_bf16 v[34:49], v[228:231], v[160:163], v[34:49]
	v_exp_f32_e32 v170, v100
	v_exp_f32_e32 v171, v101
	v_exp_f32_e32 v172, v102
	v_exp_f32_e32 v173, v103
	v_mfma_f32_32x32x16_bf16 v[34:49], v[232:235], v[66:69], v[34:49]
	v_exp_f32_e32 v174, v104
	v_exp_f32_e32 v175, v105
	v_exp_f32_e32 v176, v106
	v_exp_f32_e32 v177, v107
	v_exp_f32_e32 v178, v108
	v_mfma_f32_32x32x16_bf16 v[34:49], v[236:239], v[70:73], v[34:49]
	v_exp_f32_e32 v179, v109
	v_exp_f32_e32 v180, v110
	v_exp_f32_e32 v181, v111
	v_exp_f32_e32 v182, v112
	v_exp_f32_e32 v183, v113
	s_waitcnt lgkmcnt(0)
	s_barrier
; #define LAS __attribute__((address_space(3)))
; __device__ __forceinline__ void finishSM(f32x16& p0, f32x16& p1, float alpha, float& l_reg, bf16x8& pa0, bf16x8& pa1, bf16x8& pa2, bf16x8& pa3) {
; #pragma unroll
;     for (int r = 0; r < 16; ++r) p1[r] = EXP_PROBE ? fmaf(p1[r], 0.001f, 1.f) : __builtin_amdgcn_exp2f(p1[r]);
;     float ps = 0.f;
; #pragma unroll
;     for (int r = 0; r < 16; ++r) ps += p0[r];
; #pragma unroll
;     for (int r = 0; r < 16; ++r) ps += p1[r];
;     { auto rr = __builtin_amdgcn_permlane32_swap(__float_as_uint(ps), __float_as_uint(ps), false, false);
;       ps = __uint_as_float(rr[0]) + __uint_as_float(rr[1]); }
;     l_reg = l_reg * alpha + ps;
;     ATT_PKN(p0, 0, pa0); ATT_PKN(p0, 8, pa1); ATT_PKN(p1, 0, pa2); ATT_PKN(p1, 8, pa3);
; }
; template <int DQK> __device__ __forceinline__ void qkt(f32x16& p0, f32x16& p1, const LAS char* buf, const bf16x8* qr, int r32, int hi, const f32x16& negm) {
; #pragma unroll
;     for (int d0 = 0; d0 < 4; ++d0) { const int ch = d0 * 2 + hi;
;         const bf16x8 b0 = *(const LAS bf16x8*)(buf + B_KN + swz64(r32, ch));
;         const bf16x8 b1 = *(const LAS bf16x8*)(buf + B_KN + swz64(32 + r32, ch));
;         p0 = __builtin_amdgcn_mfma_f32_32x32x16_bf16(b0, qr[d0], d0 == 0 ? negm : p0, 0, 0, 0);
;         p1 = __builtin_amdgcn_mfma_f32_32x32x16_bf16(b1, qr[d0], d0 == 0 ? negm : p1, 0, 0, 0); }
; template <bool FIXM> __device__ __forceinline__ void pv_psm(f32x16& o0, f32x16& o1, unsigned vb, bf16x8 pa0, bf16x8 pa1, bf16x8 pa2, bf16x8 pa3,
;                                        f32x16& p0, f32x16& p1, float& m_reg, f32x16& negm, float& alpha) {
;     { const s16x4 l0 = tr_read<v_rd_off(0, 0, 0)>(vb), h0 = tr_read<v_rd_off(0, 0, 1)>(vb), l1 = tr_read<v_rd_off(0, 1, 0)>(vb), h1 = tr_read<v_rd_off(0, 1, 1)>(vb);
;       const s16x4 l2 = tr_read<v_rd_off(0, 2, 0)>(vb), h2 = tr_read<v_rd_off(0, 2, 1)>(vb), l3 = tr_read<v_rd_off(0, 3, 0)>(vb), h3 = tr_read<v_rd_off(0, 3, 1)>(vb);
;       float pmax = 0.f; SBAR(); if (!FIXM) pmax = psm_max(p0, p1); else { _Pragma("unroll") for (int r = 0; r < 8; ++r) p0[r] = __builtin_amdgcn_exp2f(p0[r]); } SBAR();
;       asm volatile("s_waitcnt lgkmcnt(0)" ::: "memory"); SBAR();
;       o0 = __builtin_amdgcn_mfma_f32_32x32x16_bf16(ATT_PK(l0, h0), pa0, o0, 0, 0, 0);
;       o0 = __builtin_amdgcn_mfma_f32_32x32x16_bf16(ATT_PK(l1, h1), pa1, o0, 0, 0, 0);
	ds_read_b128 v[224:227], v223 offset:20480
	ds_read_b128 v[228:231], v223 offset:24576
	ds_read_b128 v[232:235], v252 offset:20480
	ds_read_b128 v[236:239], v252 offset:24576
	ds_read_b128 v[240:243], v253 offset:20480
	ds_read_b128 v[244:247], v253 offset:24576
	ds_read_b128 v[248:251], v2 offset:20480
	v_exp_f32_e32 v82, v82
	v_exp_f32_e32 v83, v83
	v_exp_f32_e32 v84, v84
	v_exp_f32_e32 v85, v85
	v_exp_f32_e32 v86, v86
	v_exp_f32_e32 v87, v87
	v_exp_f32_e32 v88, v88
	v_exp_f32_e32 v89, v89
	s_waitcnt lgkmcnt(6)
	v_mfma_f32_32x32x16_bf16 v[98:113], v[224:227], v[114:117], v[18:33]
	ds_read_b128 v[224:227], v2 offset:24576
	v_exp_f32_e32 v90, v90
	v_exp_f32_e32 v91, v91
	v_exp_f32_e32 v92, v92
	v_cvt_pk_bf16_f32 v156, v168, v169
	v_cvt_pk_bf16_f32 v157, v170, v171
	v_add_f32_e32 v164, 0, v168
	v_add_f32_e32 v164, v169, v164
	v_add_f32_e32 v164, v170, v164
	s_waitcnt lgkmcnt(6)
	v_mfma_f32_32x32x16_bf16 v[66:81], v[228:231], v[114:117], v[18:33]
	v_exp_f32_e32 v93, v93
	v_exp_f32_e32 v94, v94
	v_exp_f32_e32 v95, v95
	v_cvt_pk_bf16_f32 v158, v172, v173
	v_cvt_pk_bf16_f32 v159, v174, v175
	v_add_f32_e32 v164, v171, v164
	v_add_f32_e32 v164, v172, v164
	v_add_f32_e32 v164, v173, v164
	s_waitcnt lgkmcnt(5)
	v_mfma_f32_32x32x16_bf16 v[98:113], v[232:235], v[12:15], v[98:113]
	v_exp_f32_e32 v96, v96
	v_exp_f32_e32 v97, v97
	v_cvt_pk_bf16_f32 v160, v176, v177
	v_cvt_pk_bf16_f32 v161, v178, v179
	v_cvt_pk_bf16_f32 v162, v180, v181
	v_cvt_pk_bf16_f32 v163, v182, v183
	v_add_f32_e32 v164, v174, v164
	v_add_f32_e32 v164, v175, v164
	v_add_f32_e32 v164, v176, v164
	s_waitcnt lgkmcnt(4)
	v_mfma_f32_32x32x16_bf16 v[66:81], v[236:239], v[12:15], v[66:81]
	v_add_f32_e32 v164, v177, v164
	v_add_f32_e32 v164, v178, v164
	v_add_f32_e32 v164, v179, v164
	v_add_f32_e32 v164, v180, v164
	v_add_f32_e32 v164, v181, v164
	v_add_f32_e32 v164, v182, v164
	v_add_f32_e32 v164, v183, v164
	s_waitcnt lgkmcnt(3)
	v_mfma_f32_32x32x16_bf16 v[98:113], v[240:243], v[8:11], v[98:113]
	ds_read_b64_tr_b16 v[168:169], v213 offset:0
	ds_read_b64_tr_b16 v[170:171], v213 offset:1024
	ds_read_b64_tr_b16 v[172:173], v213 offset:2048
	ds_read_b64_tr_b16 v[174:175], v213 offset:3072
	v_add_f32_e32 v164, v82, v164
	v_add_f32_e32 v164, v83, v164
	v_add_f32_e32 v164, v84, v164
	v_add_f32_e32 v164, v85, v164
	s_waitcnt lgkmcnt(6)
	v_mfma_f32_32x32x16_bf16 v[66:81], v[244:247], v[8:11], v[66:81]
	ds_read_b64_tr_b16 v[176:177], v213 offset:4096
	ds_read_b64_tr_b16 v[178:179], v213 offset:5120
	ds_read_b64_tr_b16 v[180:181], v213 offset:6144
	ds_read_b64_tr_b16 v[182:183], v213 offset:7168
	v_add_f32_e32 v164, v86, v164
	v_add_f32_e32 v164, v87, v164
	v_add_f32_e32 v164, v88, v164
	v_add_f32_e32 v164, v89, v164
	s_waitcnt lgkmcnt(9)
	v_mfma_f32_32x32x16_bf16 v[98:113], v[248:251], v[4:7], v[98:113]
	v_add_f32_e32 v164, v90, v164
	v_add_f32_e32 v164, v91, v164
	v_add_f32_e32 v164, v92, v164
	v_add_f32_e32 v164, v93, v164
	s_waitcnt lgkmcnt(8)
	v_mfma_f32_32x32x16_bf16 v[66:81], v[224:227], v[4:7], v[66:81]
	ds_read_b64_tr_b16 v[224:225], v213 offset:512
	ds_read_b64_tr_b16 v[226:227], v213 offset:1536
	ds_read_b64_tr_b16 v[228:229], v213 offset:2560
	ds_read_b64_tr_b16 v[230:231], v213 offset:3584
	ds_read_b64_tr_b16 v[232:233], v213 offset:4608
	ds_read_b64_tr_b16 v[234:235], v213 offset:5632
	ds_read_b64_tr_b16 v[236:237], v213 offset:6656
	ds_read_b64_tr_b16 v[238:239], v213 offset:7680
	s_waitcnt lgkmcnt(8)
	v_mfma_f32_32x32x16_bf16 v[50:65], v[168:171], v[156:159], v[50:65]
	v_add_f32_e32 v164, v94, v164
	v_add_f32_e32 v164, v95, v164
	v_add_f32_e32 v164, v96, v164
	v_add_f32_e32 v164, v97, v164
	v_mov_b32_e32 v165, v164
	v_mfma_f32_32x32x16_bf16 v[50:65], v[172:175], v[160:163], v[50:65]
	v_cvt_pk_bf16_f32 v82, v82, v83
	v_cvt_pk_bf16_f32 v83, v84, v85
	v_cvt_pk_bf16_f32 v84, v86, v87
	v_cvt_pk_bf16_f32 v85, v88, v89
	v_cvt_pk_bf16_f32 v86, v90, v91
	v_cvt_pk_bf16_f32 v87, v92, v93
	v_cvt_pk_bf16_f32 v88, v94, v95
	v_cvt_pk_bf16_f32 v89, v96, v97
	v_permlane32_swap_b32_e32 v164, v165
	v_mfma_f32_32x32x16_bf16 v[50:65], v[176:179], v[82:85], v[50:65]
	v_mfma_f32_32x32x16_bf16 v[50:65], v[180:183], v[86:89], v[50:65]
	s_cmp_ge_u32 s13, s30
	s_cbranch_scc1 .Lgqa_b_noload_1
	s_cmp_lt_u32 s13, s31
	s_cselect_b32 s9, 0, s31
	s_cselect_b32 s35, s12, s29
	s_lshl_b32 s9, s9, 6
	s_sub_i32 s9, s35, s9
	v_add_u32_e32 v118, s9, v137
	v_ashrrev_i32_e32 v119, 31, v118
	v_lshlrev_b64 v[118:119], 8, v[118:119]
	v_lshl_add_u64 v[120:121], v[16:17], 0, v[118:119]
	v_lshl_add_u64 v[122:123], v[134:135], 0, v[118:119]
	global_load_dwordx4 v[118:121], v[120:121], off
	s_nop 0
	global_load_dwordx4 v[122:125], v[122:123], off
; #define LAS __attribute__((address_space(3)))
; __device__ __forceinline__ void finishSM(f32x16& p0, f32x16& p1, float alpha, float& l_reg, bf16x8& pa0, bf16x8& pa1, bf16x8& pa2, bf16x8& pa3) {
; #pragma unroll
;     for (int r = 0; r < 16; ++r) p1[r] = EXP_PROBE ? fmaf(p1[r], 0.001f, 1.f) : __builtin_amdgcn_exp2f(p1[r]);
;     float ps = 0.f;
; #pragma unroll
;     for (int r = 0; r < 16; ++r) ps += p0[r];
; #pragma unroll
;     for (int r = 0; r < 16; ++r) ps += p1[r];
;     { auto rr = __builtin_amdgcn_permlane32_swap(__float_as_uint(ps), __float_as_uint(ps), false, false);
;       ps = __uint_as_float(rr[0]) + __uint_as_float(rr[1]); }
;     l_reg = l_reg * alpha + ps;
;     ATT_PKN(p0, 0, pa0); ATT_PKN(p0, 8, pa1); ATT_PKN(p1, 0, pa2); ATT_PKN(p1, 8, pa3);
; }
; template <int DQK> __device__ __forceinline__ void qkt(f32x16& p0, f32x16& p1, const LAS char* buf, const bf16x8* qr, int r32, int hi, const f32x16& negm) {
; #pragma unroll
;     for (int d0 = 0; d0 < 4; ++d0) { const int ch = d0 * 2 + hi;
;         const bf16x8 b0 = *(const LAS bf16x8*)(buf + B_KN + swz64(r32, ch));
;         const bf16x8 b1 = *(const LAS bf16x8*)(buf + B_KN + swz64(32 + r32, ch));
;         p0 = __builtin_amdgcn_mfma_f32_32x32x16_bf16(b0, qr[d0], d0 == 0 ? negm : p0, 0, 0, 0);
;         p1 = __builtin_amdgcn_mfma_f32_32x32x16_bf16(b1, qr[d0], d0 == 0 ? negm : p1, 0, 0, 0); }
; template <bool FIXM> __device__ __forceinline__ void pv_psm(f32x16& o0, f32x16& o1, unsigned vb, bf16x8 pa0, bf16x8 pa1, bf16x8 pa2, bf16x8 pa3,
;                                        f32x16& p0, f32x16& p1, float& m_reg, f32x16& negm, float& alpha) {
;     { const s16x4 l0 = tr_read<v_rd_off(0, 0, 0)>(vb), h0 = tr_read<v_rd_off(0, 0, 1)>(vb), l1 = tr_read<v_rd_off(0, 1, 0)>(vb), h1 = tr_read<v_rd_off(0, 1, 1)>(vb);
;       const s16x4 l2 = tr_read<v_rd_off(0, 2, 0)>(vb), h2 = tr_read<v_rd_off(0, 2, 1)>(vb), l3 = tr_read<v_rd_off(0, 3, 0)>(vb), h3 = tr_read<v_rd_off(0, 3, 1)>(vb);
;       float pmax = 0.f; SBAR(); if (!FIXM) pmax = psm_max(p0, p1); else { _Pragma("unroll") for (int r = 0; r < 8; ++r) p0[r] = __builtin_amdgcn_exp2f(p0[r]); } SBAR();
;       asm volatile("s_waitcnt lgkmcnt(0)" ::: "memory"); SBAR();
;       o0 = __builtin_amdgcn_mfma_f32_32x32x16_bf16(ATT_PK(l0, h0), pa0, o0, 0, 0, 0);
;       o0 = __builtin_amdgcn_mfma_f32_32x32x16_bf16(ATT_PK(l1, h1), pa1, o0, 0, 0, 0);
.Lgqa_b_ld_done_1:
	s_waitcnt lgkmcnt(0)
	v_mfma_f32_32x32x16_bf16 v[34:49], v[224:227], v[156:159], v[34:49]
	s_waitcnt vmcnt(2)
	ds_write_b128 v187, v[130:133] offset:40960
	ds_write_b128 v214, v[126:129] offset:53248
	v_exp_f32_e32 v143, v98
	v_exp_f32_e32 v145, v99
	v_mfma_f32_32x32x16_bf16 v[34:49], v[228:231], v[160:163], v[34:49]
	v_exp_f32_e32 v141, v100
	v_exp_f32_e32 v144, v101
	v_exp_f32_e32 v139, v102
	v_exp_f32_e32 v142, v103
	v_mfma_f32_32x32x16_bf16 v[34:49], v[232:235], v[82:85], v[34:49]
	v_exp_f32_e32 v138, v104
	v_exp_f32_e32 v140, v105
	v_exp_f32_e32 v151, v106
	v_exp_f32_e32 v153, v107
	v_exp_f32_e32 v149, v108
	v_mfma_f32_32x32x16_bf16 v[34:49], v[236:239], v[86:89], v[34:49]
	v_exp_f32_e32 v152, v109
	v_exp_f32_e32 v147, v110
	v_exp_f32_e32 v150, v111
	v_exp_f32_e32 v146, v112
	v_exp_f32_e32 v148, v113
	v_add_f32_e32 v154, v154, v155
	v_add_f32_e32 v136, v136, v154
	v_add_f32_e32 v164, v164, v165
	v_add_f32_e32 v136, v136, v164
	s_add_i32 s13, s13, 2
	v_add_u32_e32 v137, 0x80, v137
	s_cmp_lt_u32 s8, s0
	s_cbranch_scc0 .Lgqa_exit_1
	s_waitcnt lgkmcnt(0)
	s_barrier
	ds_read_b128 v[224:227], v223 offset:40960
	ds_read_b128 v[228:231], v223 offset:45056
	ds_read_b128 v[232:235], v252 offset:40960
	ds_read_b128 v[236:239], v252 offset:45056
	ds_read_b128 v[240:243], v253 offset:40960
	ds_read_b128 v[244:247], v253 offset:45056
	ds_read_b128 v[248:251], v2 offset:40960
	v_exp_f32_e32 v66, v66
	v_exp_f32_e32 v67, v67
	v_exp_f32_e32 v68, v68
	v_exp_f32_e32 v69, v69
	v_exp_f32_e32 v70, v70
	v_exp_f32_e32 v71, v71
	v_exp_f32_e32 v72, v72
	v_exp_f32_e32 v73, v73
	s_waitcnt lgkmcnt(6)
	v_mfma_f32_32x32x16_bf16 v[98:113], v[224:227], v[114:117], v[18:33]
	ds_read_b128 v[224:227], v2 offset:45056
	v_exp_f32_e32 v74, v74
	v_exp_f32_e32 v75, v75
	v_exp_f32_e32 v76, v76
	v_cvt_pk_bf16_f32 v156, v143, v145
	v_cvt_pk_bf16_f32 v157, v141, v144
	v_add_f32_e32 v164, 0, v143
	v_add_f32_e32 v164, v145, v164
	v_add_f32_e32 v164, v141, v164
	s_waitcnt lgkmcnt(6)
	v_mfma_f32_32x32x16_bf16 v[82:97], v[228:231], v[114:117], v[18:33]
	v_exp_f32_e32 v77, v77
	v_exp_f32_e32 v78, v78
	v_exp_f32_e32 v79, v79
	v_cvt_pk_bf16_f32 v158, v139, v142
	v_cvt_pk_bf16_f32 v159, v138, v140
	v_add_f32_e32 v164, v144, v164
	v_add_f32_e32 v164, v139, v164
	v_add_f32_e32 v164, v142, v164
	s_waitcnt lgkmcnt(5)
	v_mfma_f32_32x32x16_bf16 v[98:113], v[232:235], v[12:15], v[98:113]
	v_exp_f32_e32 v80, v80
	v_exp_f32_e32 v81, v81
	v_cvt_pk_bf16_f32 v160, v151, v153
	v_cvt_pk_bf16_f32 v161, v149, v152
	v_cvt_pk_bf16_f32 v162, v147, v150
	v_cvt_pk_bf16_f32 v163, v146, v148
	v_add_f32_e32 v164, v138, v164
	v_add_f32_e32 v164, v140, v164
	v_add_f32_e32 v164, v151, v164
	s_waitcnt lgkmcnt(4)
	v_mfma_f32_32x32x16_bf16 v[82:97], v[236:239], v[12:15], v[82:97]
	v_add_f32_e32 v164, v153, v164
	v_add_f32_e32 v164, v149, v164
	v_add_f32_e32 v164, v152, v164
	v_add_f32_e32 v164, v147, v164
	v_add_f32_e32 v164, v150, v164
	v_add_f32_e32 v164, v146, v164
	v_add_f32_e32 v164, v148, v164
	s_waitcnt lgkmcnt(3)
	v_mfma_f32_32x32x16_bf16 v[98:113], v[240:243], v[8:11], v[98:113]
	ds_read_b64_tr_b16 v[138:139], v213 offset:20480
	ds_read_b64_tr_b16 v[140:141], v213 offset:21504
	ds_read_b64_tr_b16 v[142:143], v213 offset:22528
	ds_read_b64_tr_b16 v[144:145], v213 offset:23552
	v_add_f32_e32 v164, v66, v164
	v_add_f32_e32 v164, v67, v164
	v_add_f32_e32 v164, v68, v164
	v_add_f32_e32 v164, v69, v164
	s_waitcnt lgkmcnt(6)
	v_mfma_f32_32x32x16_bf16 v[82:97], v[244:247], v[8:11], v[82:97]
	ds_read_b64_tr_b16 v[146:147], v213 offset:24576
	ds_read_b64_tr_b16 v[148:149], v213 offset:25600
	ds_read_b64_tr_b16 v[150:151], v213 offset:26624
	ds_read_b64_tr_b16 v[152:153], v213 offset:27648
	v_add_f32_e32 v164, v70, v164
	v_add_f32_e32 v164, v71, v164
	v_add_f32_e32 v164, v72, v164
	v_add_f32_e32 v164, v73, v164
	s_waitcnt lgkmcnt(9)
	v_mfma_f32_32x32x16_bf16 v[98:113], v[248:251], v[4:7], v[98:113]
	v_add_f32_e32 v164, v74, v164
	v_add_f32_e32 v164, v75, v164
	v_add_f32_e32 v164, v76, v164
	v_add_f32_e32 v164, v77, v164
	s_waitcnt lgkmcnt(8)
	v_mfma_f32_32x32x16_bf16 v[82:97], v[224:227], v[4:7], v[82:97]
	ds_read_b64_tr_b16 v[224:225], v213 offset:20992
	ds_read_b64_tr_b16 v[226:227], v213 offset:22016
	ds_read_b64_tr_b16 v[228:229], v213 offset:23040
	ds_read_b64_tr_b16 v[230:231], v213 offset:24064
	ds_read_b64_tr_b16 v[232:233], v213 offset:25088
	ds_read_b64_tr_b16 v[234:235], v213 offset:26112
	ds_read_b64_tr_b16 v[236:237], v213 offset:27136
	ds_read_b64_tr_b16 v[238:239], v213 offset:28160
	s_waitcnt lgkmcnt(8)
	v_mfma_f32_32x32x16_bf16 v[50:65], v[138:141], v[156:159], v[50:65]
	v_add_f32_e32 v164, v78, v164
	v_add_f32_e32 v164, v79, v164
	v_add_f32_e32 v164, v80, v164
	v_add_f32_e32 v154, v81, v164
	v_mov_b32_e32 v155, v154
	v_mfma_f32_32x32x16_bf16 v[50:65], v[142:145], v[160:163], v[50:65]
	v_cvt_pk_bf16_f32 v66, v66, v67
	v_cvt_pk_bf16_f32 v67, v68, v69
	v_cvt_pk_bf16_f32 v68, v70, v71
	v_cvt_pk_bf16_f32 v69, v72, v73
	v_cvt_pk_bf16_f32 v70, v74, v75
	v_cvt_pk_bf16_f32 v71, v76, v77
	v_cvt_pk_bf16_f32 v72, v78, v79
	v_cvt_pk_bf16_f32 v73, v80, v81
	v_permlane32_swap_b32_e32 v154, v155
	v_mfma_f32_32x32x16_bf16 v[50:65], v[146:149], v[66:69], v[50:65]
	s_add_i32 s8, s13, -1
	s_cmp_lt_u32 s8, s31
	s_cselect_b32 s9, 0, s31
	s_cselect_b32 s35, s12, s29
	s_lshl_b32 s9, s9, 6
	s_sub_i32 s9, s35, s9
	v_add_u32_e32 v126, s9, v137
	v_subrev_u32_e32 v126, 64, v126
	v_ashrrev_i32_e32 v127, 31, v126
	v_mfma_f32_32x32x16_bf16 v[50:65], v[150:153], v[70:73], v[50:65]
	v_lshlrev_b64 v[126:127], 8, v[126:127]
	v_lshl_add_u64 v[128:129], v[16:17], 0, v[126:127]
	v_lshl_add_u64 v[126:127], v[134:135], 0, v[126:127]
	global_load_dwordx4 v[130:133], v[128:129], off
	s_nop 0
	global_load_dwordx4 v[126:129], v[126:127], off
	s_waitcnt lgkmcnt(0)
	v_mfma_f32_32x32x16_bf16 v[34:49], v[224:227], v[156:159], v[34:49]
	s_waitcnt vmcnt(2)
	ds_write_b128 v187, v[118:121] offset:0
	ds_write_b128 v214, v[122:125] offset:12288
	v_exp_f32_e32 v168, v98
	v_exp_f32_e32 v169, v99
	v_mfma_f32_32x32x16_bf16 v[34:49], v[228:231], v[160:163], v[34:49]
	v_exp_f32_e32 v170, v100
	v_exp_f32_e32 v171, v101
	v_exp_f32_e32 v172, v102
	v_exp_f32_e32 v173, v103
	v_mfma_f32_32x32x16_bf16 v[34:49], v[232:235], v[66:69], v[34:49]
	v_exp_f32_e32 v174, v104
	v_exp_f32_e32 v175, v105
	v_exp_f32_e32 v176, v106
	v_exp_f32_e32 v177, v107
	v_exp_f32_e32 v178, v108
	v_mfma_f32_32x32x16_bf16 v[34:49], v[236:239], v[70:73], v[34:49]
	v_exp_f32_e32 v179, v109
	v_exp_f32_e32 v180, v110
	v_exp_f32_e32 v181, v111
	v_exp_f32_e32 v182, v112
	v_exp_f32_e32 v183, v113
	s_waitcnt lgkmcnt(0)
	s_barrier
; #define LAS __attribute__((address_space(3)))
; __device__ __forceinline__ void finishSM(f32x16& p0, f32x16& p1, float alpha, float& l_reg, bf16x8& pa0, bf16x8& pa1, bf16x8& pa2, bf16x8& pa3) {
; #pragma unroll
;     for (int r = 0; r < 16; ++r) p1[r] = EXP_PROBE ? fmaf(p1[r], 0.001f, 1.f) : __builtin_amdgcn_exp2f(p1[r]);
;     float ps = 0.f;
; #pragma unroll
;     for (int r = 0; r < 16; ++r) ps += p0[r];
; #pragma unroll
;     for (int r = 0; r < 16; ++r) ps += p1[r];
;     { auto rr = __builtin_amdgcn_permlane32_swap(__float_as_uint(ps), __float_as_uint(ps), false, false);
;       ps = __uint_as_float(rr[0]) + __uint_as_float(rr[1]); }
;     l_reg = l_reg * alpha + ps;
;     ATT_PKN(p0, 0, pa0); ATT_PKN(p0, 8, pa1); ATT_PKN(p1, 0, pa2); ATT_PKN(p1, 8, pa3);
; }
; template <int DQK> __device__ __forceinline__ void qkt(f32x16& p0, f32x16& p1, const LAS char* buf, const bf16x8* qr, int r32, int hi, const f32x16& negm) {
; #pragma unroll
;     for (int d0 = 0; d0 < 4; ++d0) { const int ch = d0 * 2 + hi;
;         const bf16x8 b0 = *(const LAS bf16x8*)(buf + B_KN + swz64(r32, ch));
;         const bf16x8 b1 = *(const LAS bf16x8*)(buf + B_KN + swz64(32 + r32, ch));
;         p0 = __builtin_amdgcn_mfma_f32_32x32x16_bf16(b0, qr[d0], d0 == 0 ? negm : p0, 0, 0, 0);
;         p1 = __builtin_amdgcn_mfma_f32_32x32x16_bf16(b1, qr[d0], d0 == 0 ? negm : p1, 0, 0, 0); }
; template <bool FIXM> __device__ __forceinline__ void pv_psm(f32x16& o0, f32x16& o1, unsigned vb, bf16x8 pa0, bf16x8 pa1, bf16x8 pa2, bf16x8 pa3,
;                                        f32x16& p0, f32x16& p1, float& m_reg, f32x16& negm, float& alpha) {
;     { const s16x4 l0 = tr_read<v_rd_off(0, 0, 0)>(vb), h0 = tr_read<v_rd_off(0, 0, 1)>(vb), l1 = tr_read<v_rd_off(0, 1, 0)>(vb), h1 = tr_read<v_rd_off(0, 1, 1)>(vb);
;       const s16x4 l2 = tr_read<v_rd_off(0, 2, 0)>(vb), h2 = tr_read<v_rd_off(0, 2, 1)>(vb), l3 = tr_read<v_rd_off(0, 3, 0)>(vb), h3 = tr_read<v_rd_off(0, 3, 1)>(vb);
;       float pmax = 0.f; SBAR(); if (!FIXM) pmax = psm_max(p0, p1); else { _Pragma("unroll") for (int r = 0; r < 8; ++r) p0[r] = __builtin_amdgcn_exp2f(p0[r]); } SBAR();
;       asm volatile("s_waitcnt lgkmcnt(0)" ::: "memory"); SBAR();
;       o0 = __builtin_amdgcn_mfma_f32_32x32x16_bf16(ATT_PK(l0, h0), pa0, o0, 0, 0, 0);
;       o0 = __builtin_amdgcn_mfma_f32_32x32x16_bf16(ATT_PK(l1, h1), pa1, o0, 0, 0, 0);
	ds_read_b128 v[224:227], v223 offset:0
	ds_read_b128 v[228:231], v223 offset:4096
	ds_read_b128 v[232:235], v252 offset:0
	ds_read_b128 v[236:239], v252 offset:4096
	ds_read_b128 v[240:243], v253 offset:0
	ds_read_b128 v[244:247], v253 offset:4096
	ds_read_b128 v[248:251], v2 offset:0
	v_exp_f32_e32 v82, v82
	v_exp_f32_e32 v83, v83
	v_exp_f32_e32 v84, v84
	v_exp_f32_e32 v85, v85
	v_exp_f32_e32 v86, v86
	v_exp_f32_e32 v87, v87
	v_exp_f32_e32 v88, v88
	v_exp_f32_e32 v89, v89
	s_waitcnt lgkmcnt(6)
	v_mfma_f32_32x32x16_bf16 v[98:113], v[224:227], v[114:117], v[18:33]
	ds_read_b128 v[224:227], v2 offset:4096
	v_exp_f32_e32 v90, v90
	v_exp_f32_e32 v91, v91
	v_exp_f32_e32 v92, v92
	v_cvt_pk_bf16_f32 v156, v168, v169
	v_cvt_pk_bf16_f32 v157, v170, v171
	v_add_f32_e32 v164, 0, v168
	v_add_f32_e32 v164, v169, v164
	v_add_f32_e32 v164, v170, v164
	s_waitcnt lgkmcnt(6)
	v_mfma_f32_32x32x16_bf16 v[66:81], v[228:231], v[114:117], v[18:33]
	v_exp_f32_e32 v93, v93
	v_exp_f32_e32 v94, v94
	v_exp_f32_e32 v95, v95
	v_cvt_pk_bf16_f32 v158, v172, v173
	v_cvt_pk_bf16_f32 v159, v174, v175
	v_add_f32_e32 v164, v171, v164
	v_add_f32_e32 v164, v172, v164
	v_add_f32_e32 v164, v173, v164
	s_waitcnt lgkmcnt(5)
	v_mfma_f32_32x32x16_bf16 v[98:113], v[232:235], v[12:15], v[98:113]
	v_exp_f32_e32 v96, v96
	v_exp_f32_e32 v97, v97
	v_cvt_pk_bf16_f32 v160, v176, v177
	v_cvt_pk_bf16_f32 v161, v178, v179
	v_cvt_pk_bf16_f32 v162, v180, v181
	v_cvt_pk_bf16_f32 v163, v182, v183
	v_add_f32_e32 v164, v174, v164
	v_add_f32_e32 v164, v175, v164
	v_add_f32_e32 v164, v176, v164
	s_waitcnt lgkmcnt(4)
	v_mfma_f32_32x32x16_bf16 v[66:81], v[236:239], v[12:15], v[66:81]
	v_add_f32_e32 v164, v177, v164
	v_add_f32_e32 v164, v178, v164
	v_add_f32_e32 v164, v179, v164
	v_add_f32_e32 v164, v180, v164
	v_add_f32_e32 v164, v181, v164
	v_add_f32_e32 v164, v182, v164
	v_add_f32_e32 v164, v183, v164
	s_waitcnt lgkmcnt(3)
	v_mfma_f32_32x32x16_bf16 v[98:113], v[240:243], v[8:11], v[98:113]
	ds_read_b64_tr_b16 v[168:169], v213 offset:40960
	ds_read_b64_tr_b16 v[170:171], v213 offset:41984
	ds_read_b64_tr_b16 v[172:173], v213 offset:43008
	ds_read_b64_tr_b16 v[174:175], v213 offset:44032
	v_add_f32_e32 v164, v82, v164
	v_add_f32_e32 v164, v83, v164
	v_add_f32_e32 v164, v84, v164
	v_add_f32_e32 v164, v85, v164
	s_waitcnt lgkmcnt(6)
	v_mfma_f32_32x32x16_bf16 v[66:81], v[244:247], v[8:11], v[66:81]
	ds_read_b64_tr_b16 v[176:177], v213 offset:45056
	ds_read_b64_tr_b16 v[178:179], v213 offset:46080
	ds_read_b64_tr_b16 v[180:181], v213 offset:47104
	ds_read_b64_tr_b16 v[182:183], v213 offset:48128
	v_add_f32_e32 v164, v86, v164
	v_add_f32_e32 v164, v87, v164
	v_add_f32_e32 v164, v88, v164
	v_add_f32_e32 v164, v89, v164
	s_waitcnt lgkmcnt(9)
	v_mfma_f32_32x32x16_bf16 v[98:113], v[248:251], v[4:7], v[98:113]
	v_add_f32_e32 v164, v90, v164
	v_add_f32_e32 v164, v91, v164
	v_add_f32_e32 v164, v92, v164
	v_add_f32_e32 v164, v93, v164
	s_waitcnt lgkmcnt(8)
	v_mfma_f32_32x32x16_bf16 v[66:81], v[224:227], v[4:7], v[66:81]
	ds_read_b64_tr_b16 v[224:225], v213 offset:41472
	ds_read_b64_tr_b16 v[226:227], v213 offset:42496
	ds_read_b64_tr_b16 v[228:229], v213 offset:43520
	ds_read_b64_tr_b16 v[230:231], v213 offset:44544
	ds_read_b64_tr_b16 v[232:233], v213 offset:45568
	ds_read_b64_tr_b16 v[234:235], v213 offset:46592
	ds_read_b64_tr_b16 v[236:237], v213 offset:47616
	ds_read_b64_tr_b16 v[238:239], v213 offset:48640
	s_waitcnt lgkmcnt(8)
	v_mfma_f32_32x32x16_bf16 v[50:65], v[168:171], v[156:159], v[50:65]
	v_add_f32_e32 v164, v94, v164
	v_add_f32_e32 v164, v95, v164
	v_add_f32_e32 v164, v96, v164
	v_add_f32_e32 v164, v97, v164
	v_mov_b32_e32 v165, v164
	v_mfma_f32_32x32x16_bf16 v[50:65], v[172:175], v[160:163], v[50:65]
	v_cvt_pk_bf16_f32 v82, v82, v83
	v_cvt_pk_bf16_f32 v83, v84, v85
	v_cvt_pk_bf16_f32 v84, v86, v87
	v_cvt_pk_bf16_f32 v85, v88, v89
	v_cvt_pk_bf16_f32 v86, v90, v91
	v_cvt_pk_bf16_f32 v87, v92, v93
	v_cvt_pk_bf16_f32 v88, v94, v95
	v_cvt_pk_bf16_f32 v89, v96, v97
	v_permlane32_swap_b32_e32 v164, v165
	v_mfma_f32_32x32x16_bf16 v[50:65], v[176:179], v[82:85], v[50:65]
	v_mfma_f32_32x32x16_bf16 v[50:65], v[180:183], v[86:89], v[50:65]
	s_cmp_ge_u32 s13, s30
	s_cbranch_scc1 .Lgqa_b_noload_2
	s_cmp_lt_u32 s13, s31
	s_cselect_b32 s9, 0, s31
	s_cselect_b32 s35, s12, s29
	s_lshl_b32 s9, s9, 6
	s_sub_i32 s9, s35, s9
	v_add_u32_e32 v118, s9, v137
	v_ashrrev_i32_e32 v119, 31, v118
	v_lshlrev_b64 v[118:119], 8, v[118:119]
	v_lshl_add_u64 v[120:121], v[16:17], 0, v[118:119]
	v_lshl_add_u64 v[122:123], v[134:135], 0, v[118:119]
	global_load_dwordx4 v[118:121], v[120:121], off
	s_nop 0
	global_load_dwordx4 v[122:125], v[122:123], off
.Lgqa_b_ld_done_2:
	s_waitcnt lgkmcnt(0)
	v_mfma_f32_32x32x16_bf16 v[34:49], v[224:227], v[156:159], v[34:49]
	s_waitcnt vmcnt(2)
	ds_write_b128 v187, v[130:133] offset:20480
	ds_write_b128 v214, v[126:129] offset:32768
	v_exp_f32_e32 v143, v98
	v_exp_f32_e32 v145, v99
	v_mfma_f32_32x32x16_bf16 v[34:49], v[228:231], v[160:163], v[34:49]
	v_exp_f32_e32 v141, v100
	v_exp_f32_e32 v144, v101
	v_exp_f32_e32 v139, v102
	v_exp_f32_e32 v142, v103
	v_mfma_f32_32x32x16_bf16 v[34:49], v[232:235], v[82:85], v[34:49]
	v_exp_f32_e32 v138, v104
	v_exp_f32_e32 v140, v105
	v_exp_f32_e32 v151, v106
	v_exp_f32_e32 v153, v107
	v_exp_f32_e32 v149, v108
	v_mfma_f32_32x32x16_bf16 v[34:49], v[236:239], v[86:89], v[34:49]
	v_exp_f32_e32 v152, v109
	v_exp_f32_e32 v147, v110
	v_exp_f32_e32 v150, v111
	v_exp_f32_e32 v146, v112
	v_exp_f32_e32 v148, v113
	v_add_f32_e32 v154, v154, v155
	v_add_f32_e32 v136, v136, v154
	v_add_f32_e32 v164, v164, v165
	v_add_f32_e32 v136, v136, v164
	s_add_i32 s13, s13, 2
	v_add_u32_e32 v137, 0x80, v137
	s_cmp_lt_u32 s8, s0
	s_cbranch_scc1 .LBB0_497
